# 4 proportional column sweeps instead of 2 (better L2 reuse of the gather table); outputs still written after the last sweep
# speedup vs baseline: 1.1108x; 1.0531x over previous
_Z5k_hopILi0EEvPKiPK15HIP_vector_typeIiLj2EEPKS2_IjLj4EEPS6_S8_S8_PKfSB_Pf:
	s_lshr_b32 s3, s2, 3
	s_cmpk_gt_u32 s3, 156
	s_cbranch_scc1 .Lhq0_exit
	s_load_dwordx4 s[4:7], s[0:1], 0x0
	s_load_dwordx4 s[8:11], s[0:1], 0x10
	v_lshrrev_b32_e32 v2, 6, v0
	v_and_b32_e32 v3, 63, v0
	s_bfe_u32 s13, s2, 0x10002
	s_and_b32 s14, s2, 3
	v_readfirstlane_b32 s12, v2
	s_lshl_b32 s15, s3, 2
	s_add_i32 s15, s15, s12
	s_mul_i32 s15, s15, 40
	s_mul_i32 s16, s14, 25000
	s_add_i32 s15, s15, s16
	s_add_i32 s16, s16, 24960
	s_min_u32 s15, s15, s16
	s_mul_i32 s17, s13, 0x61a84
	s_waitcnt lgkmcnt(0)
	s_add_u32 s4, s4, s17
	s_addc_u32 s5, s5, 0
	s_mul_i32 s17, s13, 0x927c00
	s_add_u32 s6, s6, s17
	s_addc_u32 s7, s7, 0
	s_mul_i32 s17, s13, 0xc35000
	s_add_u32 s8, s8, s17
	s_addc_u32 s9, s9, 0
	s_add_u32 s10, s10, s17
	s_addc_u32 s11, s11, 0
	s_mul_i32 s28, s12, 6976
	s_mov_b32 s29, 0xffff80
	v_min_u32_e32 v4, 40, v3
	v_add_u32_e32 v4, s15, v4
	v_lshlrev_b32_e32 v4, 2, v4
	global_load_dword v5, v4, s[4:5]
	v_and_b32_e32 v1, 7, v0
	v_lshlrev_b32_e32 v1, 4, v1
	v_lshrrev_b32_e32 v2, 3, v3
	v_lshlrev_b32_e32 v2, 2, v2
	v_lshlrev_b32_e32 v4, 3, v3
	v_add_u32_e32 v6, s28, v4
	v_add_u32_e32 v7, 1, v3
	v_lshlrev_b32_e32 v7, 2, v7
	s_waitcnt vmcnt(0)
	v_readlane_b32 s18, v5, 0
	v_readlane_b32 s19, v5, 40
	ds_bpermute_b32 v8, v7, v5
	s_sub_i32 s20, s19, s18
	s_lshl_b32 s21, s18, 3
	s_add_u32 s22, s6, s21
	s_addc_u32 s23, s7, 0
	s_add_u32 s24, s22, 0x1000
	s_addc_u32 s25, s23, 0
	s_cmpk_gt_i32 s20, 832
	s_cbranch_scc1 .Lhq0_staged
	global_load_dwordx2 v[56:57], v4, s[22:23] offset:0 nt
	s_cmpk_le_i32 s20, 64
	s_cbranch_scc1 .Lhq0_staged
	global_load_dwordx2 v[58:59], v4, s[22:23] offset:512 nt
	s_cmpk_le_i32 s20, 128
	s_cbranch_scc1 .Lhq0_staged
	global_load_dwordx2 v[60:61], v4, s[22:23] offset:1024 nt
	s_cmpk_le_i32 s20, 192
	s_cbranch_scc1 .Lhq0_staged
	global_load_dwordx2 v[62:63], v4, s[22:23] offset:1536 nt
	s_cmpk_le_i32 s20, 256
	s_cbranch_scc1 .Lhq0_staged
	global_load_dwordx2 v[64:65], v4, s[22:23] offset:2048 nt
	s_cmpk_le_i32 s20, 320
	s_cbranch_scc1 .Lhq0_staged
	global_load_dwordx2 v[66:67], v4, s[22:23] offset:2560 nt
	s_cmpk_le_i32 s20, 384
	s_cbranch_scc1 .Lhq0_staged
	global_load_dwordx2 v[68:69], v4, s[22:23] offset:3072 nt
	s_cmpk_le_i32 s20, 448
	s_cbranch_scc1 .Lhq0_staged
	global_load_dwordx2 v[70:71], v4, s[22:23] offset:3584 nt
	s_cmpk_le_i32 s20, 512
	s_cbranch_scc1 .Lhq0_staged
	global_load_dwordx2 v[72:73], v4, s[24:25] offset:0 nt
	s_cmpk_le_i32 s20, 576
	s_cbranch_scc1 .Lhq0_staged
	global_load_dwordx2 v[74:75], v4, s[24:25] offset:512 nt
	s_cmpk_le_i32 s20, 640
	s_cbranch_scc1 .Lhq0_staged
	global_load_dwordx2 v[76:77], v4, s[24:25] offset:1024 nt
	s_cmpk_le_i32 s20, 704
	s_cbranch_scc1 .Lhq0_staged
	global_load_dwordx2 v[78:79], v4, s[24:25] offset:1536 nt
	s_cmpk_le_i32 s20, 768
	s_cbranch_scc1 .Lhq0_staged
	global_load_dwordx2 v[80:81], v4, s[24:25] offset:2048 nt
.Lhq0_staged:
	s_waitcnt lgkmcnt(0)
	v_sub_u32_e32 v8, v8, v5
	v_lshlrev_b32_e32 v8, 6, v8
	v_sub_u32_e32 v9, 63, v3
	v_or_b32_e32 v8, v8, v9
	v_cmp_gt_u32_e32 vcc, 40, v3
	s_nop 1
	v_cndmask_b32_e32 v8, 0, v8, vcc
	v_lshlrev_b32_e32 v9, 2, v3
	v_add_u32_e32 v9, s28, v9
	ds_write_b32 v9, v8
	v_mov_b32_e32 v10, s28
	v_mov_b32_e32 v11, 0
	ds_read_b128 v[12:15], v10 offset:0
	ds_read_b128 v[16:19], v10 offset:16
	s_waitcnt lgkmcnt(0)
	v_sub_u32_e32 v20, v8, v12
	v_lshrrev_b32_e32 v20, 31, v20
	v_add_u32_e32 v11, v11, v20
	v_sub_u32_e32 v20, v8, v13
	v_lshrrev_b32_e32 v20, 31, v20
	v_add_u32_e32 v11, v11, v20
	v_sub_u32_e32 v20, v8, v14
	v_lshrrev_b32_e32 v20, 31, v20
	v_add_u32_e32 v11, v11, v20
	v_sub_u32_e32 v20, v8, v15
	v_lshrrev_b32_e32 v20, 31, v20
	v_add_u32_e32 v11, v11, v20
	v_sub_u32_e32 v20, v8, v16
	v_lshrrev_b32_e32 v20, 31, v20
	v_add_u32_e32 v11, v11, v20
	v_sub_u32_e32 v20, v8, v17
	v_lshrrev_b32_e32 v20, 31, v20
	v_add_u32_e32 v11, v11, v20
	v_sub_u32_e32 v20, v8, v18
	v_lshrrev_b32_e32 v20, 31, v20
	v_add_u32_e32 v11, v11, v20
	v_sub_u32_e32 v20, v8, v19
	v_lshrrev_b32_e32 v20, 31, v20
	v_add_u32_e32 v11, v11, v20
	ds_read_b128 v[12:15], v10 offset:32
	ds_read_b128 v[16:19], v10 offset:48
	s_waitcnt lgkmcnt(0)
	v_sub_u32_e32 v20, v8, v12
	v_lshrrev_b32_e32 v20, 31, v20
	v_add_u32_e32 v11, v11, v20
	v_sub_u32_e32 v20, v8, v13
	v_lshrrev_b32_e32 v20, 31, v20
	v_add_u32_e32 v11, v11, v20
	v_sub_u32_e32 v20, v8, v14
	v_lshrrev_b32_e32 v20, 31, v20
	v_add_u32_e32 v11, v11, v20
	v_sub_u32_e32 v20, v8, v15
	v_lshrrev_b32_e32 v20, 31, v20
	v_add_u32_e32 v11, v11, v20
	v_sub_u32_e32 v20, v8, v16
	v_lshrrev_b32_e32 v20, 31, v20
	v_add_u32_e32 v11, v11, v20
	v_sub_u32_e32 v20, v8, v17
	v_lshrrev_b32_e32 v20, 31, v20
	v_add_u32_e32 v11, v11, v20
	v_sub_u32_e32 v20, v8, v18
	v_lshrrev_b32_e32 v20, 31, v20
	v_add_u32_e32 v11, v11, v20
	v_sub_u32_e32 v20, v8, v19
	v_lshrrev_b32_e32 v20, 31, v20
	v_add_u32_e32 v11, v11, v20
	ds_read_b128 v[12:15], v10 offset:64
	ds_read_b128 v[16:19], v10 offset:80
	s_waitcnt lgkmcnt(0)
	v_sub_u32_e32 v20, v8, v12
	v_lshrrev_b32_e32 v20, 31, v20
	v_add_u32_e32 v11, v11, v20
	v_sub_u32_e32 v20, v8, v13
	v_lshrrev_b32_e32 v20, 31, v20
	v_add_u32_e32 v11, v11, v20
	v_sub_u32_e32 v20, v8, v14
	v_lshrrev_b32_e32 v20, 31, v20
	v_add_u32_e32 v11, v11, v20
	v_sub_u32_e32 v20, v8, v15
	v_lshrrev_b32_e32 v20, 31, v20
	v_add_u32_e32 v11, v11, v20
	v_sub_u32_e32 v20, v8, v16
	v_lshrrev_b32_e32 v20, 31, v20
	v_add_u32_e32 v11, v11, v20
	v_sub_u32_e32 v20, v8, v17
	v_lshrrev_b32_e32 v20, 31, v20
	v_add_u32_e32 v11, v11, v20
	v_sub_u32_e32 v20, v8, v18
	v_lshrrev_b32_e32 v20, 31, v20
	v_add_u32_e32 v11, v11, v20
	v_sub_u32_e32 v20, v8, v19
	v_lshrrev_b32_e32 v20, 31, v20
	v_add_u32_e32 v11, v11, v20
	ds_read_b128 v[12:15], v10 offset:96
	ds_read_b128 v[16:19], v10 offset:112
	s_waitcnt lgkmcnt(0)
	v_sub_u32_e32 v20, v8, v12
	v_lshrrev_b32_e32 v20, 31, v20
	v_add_u32_e32 v11, v11, v20
	v_sub_u32_e32 v20, v8, v13
	v_lshrrev_b32_e32 v20, 31, v20
	v_add_u32_e32 v11, v11, v20
	v_sub_u32_e32 v20, v8, v14
	v_lshrrev_b32_e32 v20, 31, v20
	v_add_u32_e32 v11, v11, v20
	v_sub_u32_e32 v20, v8, v15
	v_lshrrev_b32_e32 v20, 31, v20
	v_add_u32_e32 v11, v11, v20
	v_sub_u32_e32 v20, v8, v16
	v_lshrrev_b32_e32 v20, 31, v20
	v_add_u32_e32 v11, v11, v20
	v_sub_u32_e32 v20, v8, v17
	v_lshrrev_b32_e32 v20, 31, v20
	v_add_u32_e32 v11, v11, v20
	v_sub_u32_e32 v20, v8, v18
	v_lshrrev_b32_e32 v20, 31, v20
	v_add_u32_e32 v11, v11, v20
	v_sub_u32_e32 v20, v8, v19
	v_lshrrev_b32_e32 v20, 31, v20
	v_add_u32_e32 v11, v11, v20
	ds_read_b128 v[12:15], v10 offset:128
	ds_read_b128 v[16:19], v10 offset:144
	s_waitcnt lgkmcnt(0)
	v_sub_u32_e32 v20, v8, v12
	v_lshrrev_b32_e32 v20, 31, v20
	v_add_u32_e32 v11, v11, v20
	v_sub_u32_e32 v20, v8, v13
	v_lshrrev_b32_e32 v20, 31, v20
	v_add_u32_e32 v11, v11, v20
	v_sub_u32_e32 v20, v8, v14
	v_lshrrev_b32_e32 v20, 31, v20
	v_add_u32_e32 v11, v11, v20
	v_sub_u32_e32 v20, v8, v15
	v_lshrrev_b32_e32 v20, 31, v20
	v_add_u32_e32 v11, v11, v20
	v_sub_u32_e32 v20, v8, v16
	v_lshrrev_b32_e32 v20, 31, v20
	v_add_u32_e32 v11, v11, v20
	v_sub_u32_e32 v20, v8, v17
	v_lshrrev_b32_e32 v20, 31, v20
	v_add_u32_e32 v11, v11, v20
	v_sub_u32_e32 v20, v8, v18
	v_lshrrev_b32_e32 v20, 31, v20
	v_add_u32_e32 v11, v11, v20
	v_sub_u32_e32 v20, v8, v19
	v_lshrrev_b32_e32 v20, 31, v20
	v_add_u32_e32 v11, v11, v20
	v_cmp_gt_u32_e32 vcc, 40, v3
	s_and_saveexec_b64 s[44:45], vcc
	v_lshlrev_b32_e32 v11, 2, v11
	v_add_u32_e32 v11, s28, v11
	ds_write_b32 v11, v3 offset:6720
	s_mov_b64 exec, s[44:45]
	v_add_u32_e32 v9, s28, v2
	ds_read_b32 v12, v9 offset:6720
	ds_read_b32 v13, v9 offset:6752
	ds_read_b32 v14, v9 offset:6784
	ds_read_b32 v15, v9 offset:6816
	ds_read_b32 v16, v9 offset:6848
	s_waitcnt lgkmcnt(0)
	v_lshlrev_b32_e32 v12, 2, v12
	v_lshlrev_b32_e32 v13, 2, v13
	v_lshlrev_b32_e32 v14, 2, v14
	v_lshlrev_b32_e32 v15, 2, v15
	v_lshlrev_b32_e32 v16, 2, v16
	ds_bpermute_b32 v46, v12, v5
	ds_bpermute_b32 v51, v12, v5 offset:4
	ds_bpermute_b32 v47, v13, v5
	ds_bpermute_b32 v52, v13, v5 offset:4
	ds_bpermute_b32 v48, v14, v5
	ds_bpermute_b32 v53, v14, v5 offset:4
	ds_bpermute_b32 v49, v15, v5
	ds_bpermute_b32 v54, v15, v5 offset:4
	ds_bpermute_b32 v50, v16, v5
	ds_bpermute_b32 v55, v16, v5 offset:4
	s_waitcnt lgkmcnt(0)
	s_cmpk_gt_i32 s20, 832
	s_cbranch_scc1 .Lhq0_fallback
	s_waitcnt vmcnt(0)
	ds_write_b64 v6, v[56:57] offset:0
	ds_write_b64 v6, v[58:59] offset:512
	ds_write_b64 v6, v[60:61] offset:1024
	ds_write_b64 v6, v[62:63] offset:1536
	ds_write_b64 v6, v[64:65] offset:2048
	ds_write_b64 v6, v[66:67] offset:2560
	ds_write_b64 v6, v[68:69] offset:3072
	ds_write_b64 v6, v[70:71] offset:3584
	ds_write_b64 v6, v[72:73] offset:4096
	ds_write_b64 v6, v[74:75] offset:4608
	ds_write_b64 v6, v[76:77] offset:5120
	ds_write_b64 v6, v[78:79] offset:5632
	ds_write_b64 v6, v[80:81] offset:6144
	s_waitcnt lgkmcnt(0)
	v_subrev_u32_e32 v46, s18, v46
	v_subrev_u32_e32 v51, s18, v51
	v_lshl_add_u32 v46, v46, 3, s28
	v_lshl_add_u32 v51, v51, 3, s28
	v_subrev_u32_e32 v47, s18, v47
	v_subrev_u32_e32 v52, s18, v52
	v_lshl_add_u32 v47, v47, 3, s28
	v_lshl_add_u32 v52, v52, 3, s28
	v_subrev_u32_e32 v48, s18, v48
	v_subrev_u32_e32 v53, s18, v53
	v_lshl_add_u32 v48, v48, 3, s28
	v_lshl_add_u32 v53, v53, 3, s28
	v_subrev_u32_e32 v49, s18, v49
	v_subrev_u32_e32 v54, s18, v54
	v_lshl_add_u32 v49, v49, 3, s28
	v_lshl_add_u32 v54, v54, 3, s28
	v_subrev_u32_e32 v50, s18, v50
	v_subrev_u32_e32 v55, s18, v55
	v_lshl_add_u32 v50, v50, 3, s28
	v_lshl_add_u32 v55, v55, 3, s28
	v_mov_b32_e32 v56, 0
	v_mov_b32_e32 v57, 0
	v_mov_b32_e32 v58, 0
	v_mov_b32_e32 v59, 0
	v_mov_b32_e32 v60, 0
	v_mov_b32_e32 v61, 0
	v_mov_b32_e32 v62, 0
	v_mov_b32_e32 v63, 0
	v_mov_b32_e32 v64, 0
	v_mov_b32_e32 v65, 0
	v_mov_b32_e32 v66, 0
	v_mov_b32_e32 v67, 0
	v_mov_b32_e32 v68, 0
	v_mov_b32_e32 v69, 0
	v_mov_b32_e32 v70, 0
	v_mov_b32_e32 v71, 0
	v_mov_b32_e32 v72, 0
	v_mov_b32_e32 v73, 0
	v_mov_b32_e32 v74, 0
	v_mov_b32_e32 v75, 0
	v_mov_b32_e32 v76, 0
	v_mov_b32_e32 v77, 0
	v_mov_b32_e32 v78, 0
	v_mov_b32_e32 v79, 0
	v_mov_b32_e32 v80, 0
	v_mov_b32_e32 v81, 0
	v_mov_b32_e32 v82, 0
	v_mov_b32_e32 v83, 0
	v_mov_b32_e32 v84, 0
	v_mov_b32_e32 v85, 0
	v_mov_b32_e32 v86, 0
	v_mov_b32_e32 v87, 0
	v_mov_b32_e32 v88, 0
	v_mov_b32_e32 v89, 0
	v_mov_b32_e32 v90, 0
	v_mov_b32_e32 v91, 0
	v_mov_b32_e32 v92, 0
	v_mov_b32_e32 v93, 0
	v_mov_b32_e32 v94, 0
	v_mov_b32_e32 v95, 0
	s_mov_b32 s27, 4
.Lhq0_phase:
	s_mov_b32 s26, 0x8000
	s_cmp_eq_u32 s27, 3
	s_cselect_b32 s26, 0x5556, s26
	s_cmp_eq_u32 s27, 4
	s_cselect_b32 s26, 0x4000, s26
	v_sub_u32_e32 v2, v51, v46
	v_lshrrev_b32_e32 v2, 3, v2
	v_mul_u32_u24_e32 v2, s26, v2
	v_lshrrev_b32_e32 v2, 16, v2
	v_lshl_add_u32 v5, v2, 3, v46

.Lhq0_s4_done:
	s_mov_b64 exec, -1
	s_sub_i32 s27, s27, 1
	s_cmp_gt_u32 s27, 1
	s_cbranch_scc1 .Lhq0_phase
	v_mov_b32_e32 v5, v51

.Lhq0_l0_done:
	s_mov_b64 exec, -1
	v_mov_b32_e32 v5, v52

.Lhq0_l1_done:
	s_mov_b64 exec, -1
	v_mov_b32_e32 v5, v53

.Lhq0_l2_done:
	s_mov_b64 exec, -1
	v_mov_b32_e32 v5, v54

.Lhq0_l3_done:
	s_mov_b64 exec, -1
	v_mov_b32_e32 v5, v55

.Lhq0_l4_done:
	s_mov_b64 exec, -1
.Lhq0_epilogue:
	v_bfe_u32 v2, v0, 3, 3
	v_lshlrev_b32_e32 v2, 2, v2
	v_add_u32_e32 v2, s28, v2
	ds_read_b32 v46, v2 offset:6720
	ds_read_b32 v47, v2 offset:6752
	ds_read_b32 v48, v2 offset:6784
	ds_read_b32 v49, v2 offset:6816
	ds_read_b32 v50, v2 offset:6848
	s_waitcnt lgkmcnt(0)
	v_add_u32_e32 v46, s15, v46
	v_add_u32_e32 v47, s15, v47
	v_add_u32_e32 v48, s15, v48
	v_add_u32_e32 v49, s15, v49
	v_add_u32_e32 v50, s15, v50
	v_lshlrev_b32_e32 v51, 7, v46
	v_or_b32_e32 v51, v51, v1
	v_cvt_pk_f16_f32 v18, v56, v57
	v_cvt_pk_f16_f32 v19, v58, v59
	v_cvt_pk_f16_f32 v20, v60, v61
	v_cvt_pk_f16_f32 v21, v62, v63
	global_store_dwordx4 v51, v[18:21], s[10:11] nt
	v_lshlrev_b32_e32 v52, 7, v47
	v_or_b32_e32 v52, v52, v1
	v_cvt_pk_f16_f32 v22, v64, v65
	v_cvt_pk_f16_f32 v23, v66, v67
	v_cvt_pk_f16_f32 v24, v68, v69
	v_cvt_pk_f16_f32 v25, v70, v71
	global_store_dwordx4 v52, v[22:25], s[10:11] nt
	v_lshlrev_b32_e32 v53, 7, v48
	v_or_b32_e32 v53, v53, v1
	v_cvt_pk_f16_f32 v26, v72, v73
	v_cvt_pk_f16_f32 v27, v74, v75
	v_cvt_pk_f16_f32 v28, v76, v77
	v_cvt_pk_f16_f32 v29, v78, v79
	global_store_dwordx4 v53, v[26:29], s[10:11] nt
	v_lshlrev_b32_e32 v54, 7, v49
	v_or_b32_e32 v54, v54, v1
	v_cvt_pk_f16_f32 v30, v80, v81
	v_cvt_pk_f16_f32 v31, v82, v83
	v_cvt_pk_f16_f32 v32, v84, v85
	v_cvt_pk_f16_f32 v33, v86, v87
	global_store_dwordx4 v54, v[30:33], s[10:11] nt
	v_lshlrev_b32_e32 v55, 7, v50
	v_or_b32_e32 v55, v55, v1
	v_cvt_pk_f16_f32 v34, v88, v89
	v_cvt_pk_f16_f32 v35, v90, v91
	v_cvt_pk_f16_f32 v36, v92, v93
	v_cvt_pk_f16_f32 v37, v94, v95
	global_store_dwordx4 v55, v[34:37], s[10:11] nt

_Z5k_hopILi1EEvPKiPK15HIP_vector_typeIiLj2EEPKS2_IjLj4EEPS6_S8_S8_PKfSB_Pf:
	s_lshr_b32 s3, s2, 3
	s_cmpk_gt_u32 s3, 156
	s_cbranch_scc1 .Lhq1_exit
	s_load_dwordx4 s[4:7], s[0:1], 0x0
	s_load_dwordx4 s[8:11], s[0:1], 0x10
	s_load_dwordx4 s[48:51], s[0:1], 0x20
	s_load_dwordx4 s[52:55], s[0:1], 0x30
	s_load_dwordx2 s[56:57], s[0:1], 0x40
	v_lshrrev_b32_e32 v2, 6, v0
	v_and_b32_e32 v3, 63, v0
	s_bfe_u32 s13, s2, 0x10002
	s_and_b32 s14, s2, 3
	v_readfirstlane_b32 s12, v2
	s_lshl_b32 s15, s3, 2
	s_add_i32 s15, s15, s12
	s_mul_i32 s15, s15, 40
	s_mul_i32 s16, s14, 25000
	s_add_i32 s15, s15, s16
	s_add_i32 s16, s16, 24960
	s_min_u32 s15, s15, s16
	s_mul_i32 s17, s13, 0x61a84
	s_waitcnt lgkmcnt(0)
	s_add_u32 s4, s4, s17
	s_addc_u32 s5, s5, 0
	s_mul_i32 s17, s13, 0x927c00
	s_add_u32 s6, s6, s17
	s_addc_u32 s7, s7, 0
	s_mul_i32 s17, s13, 0xc35000
	s_add_u32 s8, s8, s17
	s_addc_u32 s9, s9, 0
	s_add_u32 s48, s48, s17
	s_addc_u32 s49, s49, 0
	s_add_u32 s50, s50, s17
	s_addc_u32 s51, s51, 0
	s_cmp_eq_u32 s13, 0
	s_cselect_b32 s58, s52, s54
	s_cselect_b32 s59, s53, s55
	s_load_dwordx4 s[52:55], s[58:59], 0x0
	s_lshl_b32 s17, s13, 8
	s_add_u32 s56, s56, s17
	s_addc_u32 s57, s57, 0
	s_mul_i32 s28, s12, 6976
	s_mov_b32 s29, 0xffff80
	v_min_u32_e32 v4, 40, v3
	v_add_u32_e32 v4, s15, v4
	v_lshlrev_b32_e32 v4, 2, v4
	global_load_dword v5, v4, s[4:5]
	v_and_b32_e32 v1, 7, v0
	v_lshlrev_b32_e32 v1, 4, v1
	v_lshrrev_b32_e32 v2, 3, v3
	v_lshlrev_b32_e32 v2, 2, v2
	v_lshlrev_b32_e32 v4, 3, v3
	v_add_u32_e32 v6, s28, v4
	v_add_u32_e32 v7, 1, v3
	v_lshlrev_b32_e32 v7, 2, v7
	s_waitcnt vmcnt(0)
	v_readlane_b32 s18, v5, 0
	v_readlane_b32 s19, v5, 40
	ds_bpermute_b32 v8, v7, v5
	s_sub_i32 s20, s19, s18
	s_lshl_b32 s21, s18, 3
	s_add_u32 s22, s6, s21
	s_addc_u32 s23, s7, 0
	s_add_u32 s24, s22, 0x1000
	s_addc_u32 s25, s23, 0
	s_cmpk_gt_i32 s20, 832
	s_cbranch_scc1 .Lhq1_staged
	global_load_dwordx2 v[56:57], v4, s[22:23] offset:0 nt
	s_cmpk_le_i32 s20, 64
	s_cbranch_scc1 .Lhq1_staged
	global_load_dwordx2 v[58:59], v4, s[22:23] offset:512 nt
	s_cmpk_le_i32 s20, 128
	s_cbranch_scc1 .Lhq1_staged
	global_load_dwordx2 v[60:61], v4, s[22:23] offset:1024 nt
	s_cmpk_le_i32 s20, 192
	s_cbranch_scc1 .Lhq1_staged
	global_load_dwordx2 v[62:63], v4, s[22:23] offset:1536 nt
	s_cmpk_le_i32 s20, 256
	s_cbranch_scc1 .Lhq1_staged
	global_load_dwordx2 v[64:65], v4, s[22:23] offset:2048 nt
	s_cmpk_le_i32 s20, 320
	s_cbranch_scc1 .Lhq1_staged
	global_load_dwordx2 v[66:67], v4, s[22:23] offset:2560 nt
	s_cmpk_le_i32 s20, 384
	s_cbranch_scc1 .Lhq1_staged
	global_load_dwordx2 v[68:69], v4, s[22:23] offset:3072 nt
	s_cmpk_le_i32 s20, 448
	s_cbranch_scc1 .Lhq1_staged
	global_load_dwordx2 v[70:71], v4, s[22:23] offset:3584 nt
	s_cmpk_le_i32 s20, 512
	s_cbranch_scc1 .Lhq1_staged
	global_load_dwordx2 v[72:73], v4, s[24:25] offset:0 nt
	s_cmpk_le_i32 s20, 576
	s_cbranch_scc1 .Lhq1_staged
	global_load_dwordx2 v[74:75], v4, s[24:25] offset:512 nt
	s_cmpk_le_i32 s20, 640
	s_cbranch_scc1 .Lhq1_staged
	global_load_dwordx2 v[76:77], v4, s[24:25] offset:1024 nt
	s_cmpk_le_i32 s20, 704
	s_cbranch_scc1 .Lhq1_staged
	global_load_dwordx2 v[78:79], v4, s[24:25] offset:1536 nt
	s_cmpk_le_i32 s20, 768
	s_cbranch_scc1 .Lhq1_staged
	global_load_dwordx2 v[80:81], v4, s[24:25] offset:2048 nt

.Lhq1_l4_done:
	s_mov_b64 exec, -1
.Lhq1_epilogue:
	v_bfe_u32 v2, v0, 3, 3
	v_lshlrev_b32_e32 v2, 2, v2
	v_add_u32_e32 v2, s28, v2
	ds_read_b32 v46, v2 offset:6720
	ds_read_b32 v47, v2 offset:6752
	ds_read_b32 v48, v2 offset:6784
	ds_read_b32 v49, v2 offset:6816
	ds_read_b32 v50, v2 offset:6848
	s_waitcnt lgkmcnt(0)
	v_add_u32_e32 v46, s15, v46
	v_add_u32_e32 v47, s15, v47
	v_add_u32_e32 v48, s15, v48
	v_add_u32_e32 v49, s15, v49
	v_add_u32_e32 v50, s15, v50
	s_mov_b32 s46, s55
	v_lshlrev_b32_e32 v3, 7, v46
	v_or_b32_e32 v3, v3, v1
	global_load_dwordx4 v[6:9], v3, s[48:49] nt
	global_load_dwordx4 v[10:13], v3, s[50:51] nt
	global_load_dwordx4 v[14:17], v3, s[8:9]
	v_lshlrev_b32_e32 v4, 7, v47
	v_or_b32_e32 v4, v4, v1
	global_load_dwordx4 v[18:21], v4, s[48:49] nt
	global_load_dwordx4 v[22:25], v4, s[50:51] nt
	global_load_dwordx4 v[26:29], v4, s[8:9]
	s_waitcnt vmcnt(3)
	v_cvt_f32_f16_e32 v38, v6
	v_cvt_f32_f16_sdwa v39, v6 dst_sel:DWORD dst_unused:UNUSED_PAD src0_sel:WORD_1
	v_cvt_f32_f16_e32 v40, v8
	v_cvt_f32_f16_sdwa v41, v8 dst_sel:DWORD dst_unused:UNUSED_PAD src0_sel:WORD_1
	v_cvt_f32_f16_e32 v6, v7
	v_cvt_f32_f16_sdwa v7, v7 dst_sel:DWORD dst_unused:UNUSED_PAD src0_sel:WORD_1
	v_cvt_f32_f16_e32 v8, v9
	v_cvt_f32_f16_sdwa v9, v9 dst_sel:DWORD dst_unused:UNUSED_PAD src0_sel:WORD_1
	v_mul_f32_e32 v30, s52, v38
	v_mul_f32_e32 v31, s52, v39
	v_mul_f32_e32 v32, s52, v6
	v_mul_f32_e32 v33, s52, v7
	v_mul_f32_e32 v34, s52, v40
	v_mul_f32_e32 v35, s52, v41
	v_mul_f32_e32 v36, s52, v8
	v_mul_f32_e32 v37, s52, v9
	v_cvt_f32_f16_e32 v38, v10
	v_cvt_f32_f16_sdwa v39, v10 dst_sel:DWORD dst_unused:UNUSED_PAD src0_sel:WORD_1
	v_cvt_f32_f16_e32 v40, v12
	v_cvt_f32_f16_sdwa v41, v12 dst_sel:DWORD dst_unused:UNUSED_PAD src0_sel:WORD_1
	v_cvt_f32_f16_e32 v10, v11
	v_cvt_f32_f16_sdwa v11, v11 dst_sel:DWORD dst_unused:UNUSED_PAD src0_sel:WORD_1
	v_cvt_f32_f16_e32 v12, v13
	v_cvt_f32_f16_sdwa v13, v13 dst_sel:DWORD dst_unused:UNUSED_PAD src0_sel:WORD_1
	v_fma_f32 v30, s53, v38, v30
	v_fma_f32 v31, s53, v39, v31
	v_fma_f32 v32, s53, v10, v32
	v_fma_f32 v33, s53, v11, v33
	v_fma_f32 v34, s53, v40, v34
	v_fma_f32 v35, s53, v41, v35
	v_fma_f32 v36, s53, v12, v36
	v_fma_f32 v37, s53, v13, v37
	v_cvt_f32_f16_e32 v38, v14
	v_cvt_f32_f16_sdwa v39, v14 dst_sel:DWORD dst_unused:UNUSED_PAD src0_sel:WORD_1
	v_cvt_f32_f16_e32 v40, v16
	v_cvt_f32_f16_sdwa v41, v16 dst_sel:DWORD dst_unused:UNUSED_PAD src0_sel:WORD_1
	v_cvt_f32_f16_e32 v14, v15
	v_cvt_f32_f16_sdwa v15, v15 dst_sel:DWORD dst_unused:UNUSED_PAD src0_sel:WORD_1
	v_cvt_f32_f16_e32 v16, v17
	v_cvt_f32_f16_sdwa v17, v17 dst_sel:DWORD dst_unused:UNUSED_PAD src0_sel:WORD_1
	v_fma_f32 v30, s54, v38, v30
	v_fma_f32 v31, s54, v39, v31
	v_fma_f32 v32, s54, v14, v32
	v_fma_f32 v33, s54, v15, v33
	v_fma_f32 v34, s54, v40, v34
	v_fma_f32 v35, s54, v41, v35
	v_fma_f32 v36, s54, v16, v36
	v_fma_f32 v37, s54, v17, v37
	v_fma_f32 v30, s46, v56, v30
	v_fma_f32 v31, s46, v57, v31
	v_fma_f32 v32, s46, v58, v32
	v_fma_f32 v33, s46, v59, v33
	v_fma_f32 v34, s46, v60, v34
	v_fma_f32 v35, s46, v61, v35
	v_fma_f32 v36, s46, v62, v36
	v_fma_f32 v37, s46, v63, v37
	v_lshlrev_b32_e32 v46, 9, v46
	v_or_b32_e32 v46, v46, v1
	global_store_dwordx4 v46, v[30:33], s[56:57] nt
	global_store_dwordx4 v46, v[34:37], s[56:57] offset:128 nt
	v_lshlrev_b32_e32 v3, 7, v48
	v_or_b32_e32 v3, v3, v1
	global_load_dwordx4 v[6:9], v3, s[48:49] nt
	global_load_dwordx4 v[10:13], v3, s[50:51] nt
	global_load_dwordx4 v[14:17], v3, s[8:9]
	s_waitcnt vmcnt(5)
	v_cvt_f32_f16_e32 v38, v18
	v_cvt_f32_f16_sdwa v39, v18 dst_sel:DWORD dst_unused:UNUSED_PAD src0_sel:WORD_1
	v_cvt_f32_f16_e32 v40, v20
	v_cvt_f32_f16_sdwa v41, v20 dst_sel:DWORD dst_unused:UNUSED_PAD src0_sel:WORD_1
	v_cvt_f32_f16_e32 v18, v19
	v_cvt_f32_f16_sdwa v19, v19 dst_sel:DWORD dst_unused:UNUSED_PAD src0_sel:WORD_1
	v_cvt_f32_f16_e32 v20, v21
	v_cvt_f32_f16_sdwa v21, v21 dst_sel:DWORD dst_unused:UNUSED_PAD src0_sel:WORD_1
	v_mul_f32_e32 v30, s52, v38
	v_mul_f32_e32 v31, s52, v39
	v_mul_f32_e32 v32, s52, v18
	v_mul_f32_e32 v33, s52, v19
	v_mul_f32_e32 v34, s52, v40
	v_mul_f32_e32 v35, s52, v41
	v_mul_f32_e32 v36, s52, v20
	v_mul_f32_e32 v37, s52, v21
	v_cvt_f32_f16_e32 v38, v22
	v_cvt_f32_f16_sdwa v39, v22 dst_sel:DWORD dst_unused:UNUSED_PAD src0_sel:WORD_1
	v_cvt_f32_f16_e32 v40, v24
	v_cvt_f32_f16_sdwa v41, v24 dst_sel:DWORD dst_unused:UNUSED_PAD src0_sel:WORD_1
	v_cvt_f32_f16_e32 v22, v23
	v_cvt_f32_f16_sdwa v23, v23 dst_sel:DWORD dst_unused:UNUSED_PAD src0_sel:WORD_1
	v_cvt_f32_f16_e32 v24, v25
	v_cvt_f32_f16_sdwa v25, v25 dst_sel:DWORD dst_unused:UNUSED_PAD src0_sel:WORD_1
	v_fma_f32 v30, s53, v38, v30
	v_fma_f32 v31, s53, v39, v31
	v_fma_f32 v32, s53, v22, v32
	v_fma_f32 v33, s53, v23, v33
	v_fma_f32 v34, s53, v40, v34
	v_fma_f32 v35, s53, v41, v35
	v_fma_f32 v36, s53, v24, v36
	v_fma_f32 v37, s53, v25, v37
	v_cvt_f32_f16_e32 v38, v26
	v_cvt_f32_f16_sdwa v39, v26 dst_sel:DWORD dst_unused:UNUSED_PAD src0_sel:WORD_1
	v_cvt_f32_f16_e32 v40, v28
	v_cvt_f32_f16_sdwa v41, v28 dst_sel:DWORD dst_unused:UNUSED_PAD src0_sel:WORD_1
	v_cvt_f32_f16_e32 v26, v27
	v_cvt_f32_f16_sdwa v27, v27 dst_sel:DWORD dst_unused:UNUSED_PAD src0_sel:WORD_1
	v_cvt_f32_f16_e32 v28, v29
	v_cvt_f32_f16_sdwa v29, v29 dst_sel:DWORD dst_unused:UNUSED_PAD src0_sel:WORD_1
	v_fma_f32 v30, s54, v38, v30
	v_fma_f32 v31, s54, v39, v31
	v_fma_f32 v32, s54, v26, v32
	v_fma_f32 v33, s54, v27, v33
	v_fma_f32 v34, s54, v40, v34
	v_fma_f32 v35, s54, v41, v35
	v_fma_f32 v36, s54, v28, v36
	v_fma_f32 v37, s54, v29, v37
	v_fma_f32 v30, s46, v64, v30
	v_fma_f32 v31, s46, v65, v31
	v_fma_f32 v32, s46, v66, v32
	v_fma_f32 v33, s46, v67, v33
	v_fma_f32 v34, s46, v68, v34
	v_fma_f32 v35, s46, v69, v35
	v_fma_f32 v36, s46, v70, v36
	v_fma_f32 v37, s46, v71, v37
	v_lshlrev_b32_e32 v47, 9, v47
	v_or_b32_e32 v47, v47, v1
	global_store_dwordx4 v47, v[30:33], s[56:57] nt
	global_store_dwordx4 v47, v[34:37], s[56:57] offset:128 nt
	v_lshlrev_b32_e32 v4, 7, v49
	v_or_b32_e32 v4, v4, v1
	global_load_dwordx4 v[18:21], v4, s[48:49] nt
	global_load_dwordx4 v[22:25], v4, s[50:51] nt
	global_load_dwordx4 v[26:29], v4, s[8:9]
	s_waitcnt vmcnt(5)
	v_cvt_f32_f16_e32 v38, v6
	v_cvt_f32_f16_sdwa v39, v6 dst_sel:DWORD dst_unused:UNUSED_PAD src0_sel:WORD_1
	v_cvt_f32_f16_e32 v40, v8
	v_cvt_f32_f16_sdwa v41, v8 dst_sel:DWORD dst_unused:UNUSED_PAD src0_sel:WORD_1
	v_cvt_f32_f16_e32 v6, v7
	v_cvt_f32_f16_sdwa v7, v7 dst_sel:DWORD dst_unused:UNUSED_PAD src0_sel:WORD_1
	v_cvt_f32_f16_e32 v8, v9
	v_cvt_f32_f16_sdwa v9, v9 dst_sel:DWORD dst_unused:UNUSED_PAD src0_sel:WORD_1
	v_mul_f32_e32 v30, s52, v38
	v_mul_f32_e32 v31, s52, v39
	v_mul_f32_e32 v32, s52, v6
	v_mul_f32_e32 v33, s52, v7
	v_mul_f32_e32 v34, s52, v40
	v_mul_f32_e32 v35, s52, v41
	v_mul_f32_e32 v36, s52, v8
	v_mul_f32_e32 v37, s52, v9
	v_cvt_f32_f16_e32 v38, v10
	v_cvt_f32_f16_sdwa v39, v10 dst_sel:DWORD dst_unused:UNUSED_PAD src0_sel:WORD_1
	v_cvt_f32_f16_e32 v40, v12
	v_cvt_f32_f16_sdwa v41, v12 dst_sel:DWORD dst_unused:UNUSED_PAD src0_sel:WORD_1
	v_cvt_f32_f16_e32 v10, v11
	v_cvt_f32_f16_sdwa v11, v11 dst_sel:DWORD dst_unused:UNUSED_PAD src0_sel:WORD_1
	v_cvt_f32_f16_e32 v12, v13
	v_cvt_f32_f16_sdwa v13, v13 dst_sel:DWORD dst_unused:UNUSED_PAD src0_sel:WORD_1
	v_fma_f32 v30, s53, v38, v30
	v_fma_f32 v31, s53, v39, v31
	v_fma_f32 v32, s53, v10, v32
	v_fma_f32 v33, s53, v11, v33
	v_fma_f32 v34, s53, v40, v34
	v_fma_f32 v35, s53, v41, v35
	v_fma_f32 v36, s53, v12, v36
	v_fma_f32 v37, s53, v13, v37
	v_cvt_f32_f16_e32 v38, v14
	v_cvt_f32_f16_sdwa v39, v14 dst_sel:DWORD dst_unused:UNUSED_PAD src0_sel:WORD_1
	v_cvt_f32_f16_e32 v40, v16
	v_cvt_f32_f16_sdwa v41, v16 dst_sel:DWORD dst_unused:UNUSED_PAD src0_sel:WORD_1
	v_cvt_f32_f16_e32 v14, v15
	v_cvt_f32_f16_sdwa v15, v15 dst_sel:DWORD dst_unused:UNUSED_PAD src0_sel:WORD_1
	v_cvt_f32_f16_e32 v16, v17
	v_cvt_f32_f16_sdwa v17, v17 dst_sel:DWORD dst_unused:UNUSED_PAD src0_sel:WORD_1
	v_fma_f32 v30, s54, v38, v30
	v_fma_f32 v31, s54, v39, v31
	v_fma_f32 v32, s54, v14, v32
	v_fma_f32 v33, s54, v15, v33
	v_fma_f32 v34, s54, v40, v34
	v_fma_f32 v35, s54, v41, v35
	v_fma_f32 v36, s54, v16, v36
	v_fma_f32 v37, s54, v17, v37
	v_fma_f32 v30, s46, v72, v30
	v_fma_f32 v31, s46, v73, v31
	v_fma_f32 v32, s46, v74, v32
	v_fma_f32 v33, s46, v75, v33
	v_fma_f32 v34, s46, v76, v34
	v_fma_f32 v35, s46, v77, v35
	v_fma_f32 v36, s46, v78, v36
	v_fma_f32 v37, s46, v79, v37
	v_lshlrev_b32_e32 v48, 9, v48
	v_or_b32_e32 v48, v48, v1
	global_store_dwordx4 v48, v[30:33], s[56:57] nt
	global_store_dwordx4 v48, v[34:37], s[56:57] offset:128 nt
	v_lshlrev_b32_e32 v3, 7, v50
	v_or_b32_e32 v3, v3, v1
	global_load_dwordx4 v[6:9], v3, s[48:49] nt
	global_load_dwordx4 v[10:13], v3, s[50:51] nt
	global_load_dwordx4 v[14:17], v3, s[8:9]
	s_waitcnt vmcnt(5)
	v_cvt_f32_f16_e32 v38, v18
	v_cvt_f32_f16_sdwa v39, v18 dst_sel:DWORD dst_unused:UNUSED_PAD src0_sel:WORD_1
	v_cvt_f32_f16_e32 v40, v20
	v_cvt_f32_f16_sdwa v41, v20 dst_sel:DWORD dst_unused:UNUSED_PAD src0_sel:WORD_1
	v_cvt_f32_f16_e32 v18, v19
	v_cvt_f32_f16_sdwa v19, v19 dst_sel:DWORD dst_unused:UNUSED_PAD src0_sel:WORD_1
	v_cvt_f32_f16_e32 v20, v21
	v_cvt_f32_f16_sdwa v21, v21 dst_sel:DWORD dst_unused:UNUSED_PAD src0_sel:WORD_1
	v_mul_f32_e32 v30, s52, v38
	v_mul_f32_e32 v31, s52, v39
	v_mul_f32_e32 v32, s52, v18
	v_mul_f32_e32 v33, s52, v19
	v_mul_f32_e32 v34, s52, v40
	v_mul_f32_e32 v35, s52, v41
	v_mul_f32_e32 v36, s52, v20
	v_mul_f32_e32 v37, s52, v21
	v_cvt_f32_f16_e32 v38, v22
	v_cvt_f32_f16_sdwa v39, v22 dst_sel:DWORD dst_unused:UNUSED_PAD src0_sel:WORD_1
	v_cvt_f32_f16_e32 v40, v24
	v_cvt_f32_f16_sdwa v41, v24 dst_sel:DWORD dst_unused:UNUSED_PAD src0_sel:WORD_1
	v_cvt_f32_f16_e32 v22, v23
	v_cvt_f32_f16_sdwa v23, v23 dst_sel:DWORD dst_unused:UNUSED_PAD src0_sel:WORD_1
	v_cvt_f32_f16_e32 v24, v25
	v_cvt_f32_f16_sdwa v25, v25 dst_sel:DWORD dst_unused:UNUSED_PAD src0_sel:WORD_1
	v_fma_f32 v30, s53, v38, v30
	v_fma_f32 v31, s53, v39, v31
	v_fma_f32 v32, s53, v22, v32
	v_fma_f32 v33, s53, v23, v33
	v_fma_f32 v34, s53, v40, v34
	v_fma_f32 v35, s53, v41, v35
	v_fma_f32 v36, s53, v24, v36
	v_fma_f32 v37, s53, v25, v37
	v_cvt_f32_f16_e32 v38, v26
	v_cvt_f32_f16_sdwa v39, v26 dst_sel:DWORD dst_unused:UNUSED_PAD src0_sel:WORD_1
	v_cvt_f32_f16_e32 v40, v28
	v_cvt_f32_f16_sdwa v41, v28 dst_sel:DWORD dst_unused:UNUSED_PAD src0_sel:WORD_1
	v_cvt_f32_f16_e32 v26, v27
	v_cvt_f32_f16_sdwa v27, v27 dst_sel:DWORD dst_unused:UNUSED_PAD src0_sel:WORD_1
	v_cvt_f32_f16_e32 v28, v29
	v_cvt_f32_f16_sdwa v29, v29 dst_sel:DWORD dst_unused:UNUSED_PAD src0_sel:WORD_1
	v_fma_f32 v30, s54, v38, v30
	v_fma_f32 v31, s54, v39, v31
	v_fma_f32 v32, s54, v26, v32
	v_fma_f32 v33, s54, v27, v33
	v_fma_f32 v34, s54, v40, v34
	v_fma_f32 v35, s54, v41, v35
	v_fma_f32 v36, s54, v28, v36
	v_fma_f32 v37, s54, v29, v37
	v_fma_f32 v30, s46, v80, v30
	v_fma_f32 v31, s46, v81, v31
	v_fma_f32 v32, s46, v82, v32
	v_fma_f32 v33, s46, v83, v33
	v_fma_f32 v34, s46, v84, v34
	v_fma_f32 v35, s46, v85, v35
	v_fma_f32 v36, s46, v86, v36
	v_fma_f32 v37, s46, v87, v37
	v_lshlrev_b32_e32 v49, 9, v49
	v_or_b32_e32 v49, v49, v1
	global_store_dwordx4 v49, v[30:33], s[56:57] nt
	global_store_dwordx4 v49, v[34:37], s[56:57] offset:128 nt
	s_waitcnt vmcnt(2)
	v_cvt_f32_f16_e32 v38, v6
	v_cvt_f32_f16_sdwa v39, v6 dst_sel:DWORD dst_unused:UNUSED_PAD src0_sel:WORD_1
	v_cvt_f32_f16_e32 v40, v8
	v_cvt_f32_f16_sdwa v41, v8 dst_sel:DWORD dst_unused:UNUSED_PAD src0_sel:WORD_1
	v_cvt_f32_f16_e32 v6, v7
	v_cvt_f32_f16_sdwa v7, v7 dst_sel:DWORD dst_unused:UNUSED_PAD src0_sel:WORD_1
	v_cvt_f32_f16_e32 v8, v9
	v_cvt_f32_f16_sdwa v9, v9 dst_sel:DWORD dst_unused:UNUSED_PAD src0_sel:WORD_1
	v_mul_f32_e32 v30, s52, v38
	v_mul_f32_e32 v31, s52, v39
	v_mul_f32_e32 v32, s52, v6
	v_mul_f32_e32 v33, s52, v7
	v_mul_f32_e32 v34, s52, v40
	v_mul_f32_e32 v35, s52, v41
	v_mul_f32_e32 v36, s52, v8
	v_mul_f32_e32 v37, s52, v9
	v_cvt_f32_f16_e32 v38, v10
	v_cvt_f32_f16_sdwa v39, v10 dst_sel:DWORD dst_unused:UNUSED_PAD src0_sel:WORD_1
	v_cvt_f32_f16_e32 v40, v12
	v_cvt_f32_f16_sdwa v41, v12 dst_sel:DWORD dst_unused:UNUSED_PAD src0_sel:WORD_1
	v_cvt_f32_f16_e32 v10, v11
	v_cvt_f32_f16_sdwa v11, v11 dst_sel:DWORD dst_unused:UNUSED_PAD src0_sel:WORD_1
	v_cvt_f32_f16_e32 v12, v13
	v_cvt_f32_f16_sdwa v13, v13 dst_sel:DWORD dst_unused:UNUSED_PAD src0_sel:WORD_1
	v_fma_f32 v30, s53, v38, v30
	v_fma_f32 v31, s53, v39, v31
	v_fma_f32 v32, s53, v10, v32
	v_fma_f32 v33, s53, v11, v33
	v_fma_f32 v34, s53, v40, v34
	v_fma_f32 v35, s53, v41, v35
	v_fma_f32 v36, s53, v12, v36
	v_fma_f32 v37, s53, v13, v37
	v_cvt_f32_f16_e32 v38, v14
	v_cvt_f32_f16_sdwa v39, v14 dst_sel:DWORD dst_unused:UNUSED_PAD src0_sel:WORD_1
	v_cvt_f32_f16_e32 v40, v16
	v_cvt_f32_f16_sdwa v41, v16 dst_sel:DWORD dst_unused:UNUSED_PAD src0_sel:WORD_1
	v_cvt_f32_f16_e32 v14, v15
	v_cvt_f32_f16_sdwa v15, v15 dst_sel:DWORD dst_unused:UNUSED_PAD src0_sel:WORD_1
	v_cvt_f32_f16_e32 v16, v17
	v_cvt_f32_f16_sdwa v17, v17 dst_sel:DWORD dst_unused:UNUSED_PAD src0_sel:WORD_1
	v_fma_f32 v30, s54, v38, v30
	v_fma_f32 v31, s54, v39, v31
	v_fma_f32 v32, s54, v14, v32
	v_fma_f32 v33, s54, v15, v33
	v_fma_f32 v34, s54, v40, v34
	v_fma_f32 v35, s54, v41, v35
	v_fma_f32 v36, s54, v16, v36
	v_fma_f32 v37, s54, v17, v37
	v_fma_f32 v30, s46, v88, v30
	v_fma_f32 v31, s46, v89, v31
	v_fma_f32 v32, s46, v90, v32
	v_fma_f32 v33, s46, v91, v33
	v_fma_f32 v34, s46, v92, v34
	v_fma_f32 v35, s46, v93, v35
	v_fma_f32 v36, s46, v94, v36
	v_fma_f32 v37, s46, v95, v37
	v_lshlrev_b32_e32 v50, 9, v50
	v_or_b32_e32 v50, v50, v1
	global_store_dwordx4 v50, v[30:33], s[56:57] nt
	global_store_dwordx4 v50, v[34:37], s[56:57] offset:128 nt
